# up-projection output: seven eighths of H stored with the default cache policy, one eighth nt
# baseline (speedup 1.0000x reference)
; #define PG8_LAS __attribute__((address_space(3)))
; #define PG8_GAS __attribute__((address_space(1)))
; #define PG8_PACK8(y0, y1) (u32x4){cvt_pk_bf16((y0)[0], (y0)[1]), cvt_pk_bf16((y0)[2], (y0)[3]), cvt_pk_bf16((y1)[0], (y1)[1]), cvt_pk_bf16((y1)[2], (y1)[3])}
;     __device__ __forceinline__ void operator()(const f32x4 (&acc)[2][2][4][2], const Unit& u, int ui, int wr, int wc, int fr, int fq) const {
;     ...
;         const unsigned row0 = (unsigned)(u.pm * BM + wr * 64 + fr), colp = (unsigned)((u.pn & 3) * BM + wc * 32 + 8 * fq);
;         const PG8_LAS float* rsp = tab + (u.pm == pmA ? 0 : 256) + wr * 64 + fr;
;         float rsv[2][4];
; #pragma unroll
;         for (int ai = 0; ai < 2; ++ai)
; #pragma unroll
;             for (int m = 0; m < 4; ++m) rsv[ai][m] = rsp[ai * HALF + m * 16];
; #pragma unroll
;         for (int ai = 0; ai < 2; ++ai)
; #pragma unroll
;             for (int m = 0; m < 4; ++m) {
;                 const unsigned row = row0 + ai * HALF + m * 16; const float rs = rsv[ai][m];
; #pragma unroll
;                 for (int bj = 0; bj < 2; ++bj) {
;                     f32x4 y0 = acc[ai][bj][m][0] * rs, y1 = acc[ai][bj][m][1] * rs;
; #pragma unroll
;                     for (int e = 0; e < 4; ++e) { const float a = fmaxf(y0[e], 0.f), b = fmaxf(y1[e], 0.f); y0[e] = a * a; y1[e] = b * b; }
;                     const u32x4 hw = PG8_PACK8(y0, y1);
;     ...
;                     if (probe_mode == 1) { asm volatile("" :: "v"(hw)); } else
;     ...
;                     *(PG8_GAS u32x4*)((PG8_GAS unsigned char*)ws + E_QKVO + (size_t)((unsigned)(u.pm >> 4) * (24u << 20) + (unsigned)(u.pn >> 2) * (8u << 20) + row * 2048u + (colp + bj * HALF) * 2u)) = hw;
;                 }
.LBB0_64:
	s_lshl_b32 s13, s51, 9
	s_cmp_eq_u32 s20, s29
	s_cselect_b32 s15, 0, 0x400
	v_add_u32_e32 v140, s15, v145
	ds_read2_b32 v[164:165], v140 offset1:16
	ds_read2_b32 v[166:167], v140 offset0:32 offset1:48
	ds_read2_b32 v[142:143], v140 offset0:128 offset1:144
	ds_read2_b32 v[140:141], v140 offset0:160 offset1:176
	s_lshl_b32 s22, s51, 21
	s_lshr_b32 s15, s20, 4
	s_and_b32 s22, s22, 0xff800000
	s_lshl_b32 s20, s20, 19
	s_waitcnt lgkmcnt(0)
	v_pk_mul_f32 v[122:123], v[122:123], v[164:165] op_sel_hi:[1,0]
	s_add_i32 s22, s22, s20
	v_pk_mul_f32 v[126:127], v[126:127], v[164:165] op_sel_hi:[1,0]
	v_pk_mul_f32 v[124:125], v[124:125], v[164:165] op_sel_hi:[1,0]
	v_max_f32_e32 v122, 0, v122
	s_and_b32 s13, s13, 0x600
	v_add_u32_e32 v163, s22, v146
	v_pk_mul_f32 v[128:129], v[128:129], v[164:165] op_sel_hi:[1,0]
	v_mul_f32_e32 v168, v122, v122
	v_max_f32_e32 v122, 0, v127
	v_max_f32_e32 v123, 0, v123
	v_max_f32_e32 v124, 0, v124
	s_mul_i32 s15, s15, 0x1800000
	v_or_b32_e32 v163, s13, v163
	v_max_f32_e32 v126, 0, v126
	v_mul_f32_e32 v122, v122, v122
	v_mul_f32_e32 v127, v123, v123
	v_max_f32_e32 v123, 0, v128
	v_mul_f32_e32 v128, v124, v124
	v_max_f32_e32 v124, 0, v129
	v_max_f32_e32 v125, 0, v125
	v_pk_mul_f32 v[114:115], v[114:115], v[164:165] op_sel_hi:[1,0]
	v_add_u32_e32 v163, s15, v163
	v_mul_f32_e32 v126, v126, v126
	v_mul_f32_e32 v123, v123, v123
	v_mul_f32_e32 v124, v124, v124
	v_mul_f32_e32 v125, v125, v125
	v_cvt_pk_bf16_f32 v122, v126, v122
	v_pk_mul_f32 v[120:121], v[120:121], v[164:165] op_sel_hi:[1,0]
	v_pk_mul_f32 v[118:119], v[118:119], v[164:165] op_sel_hi:[1,0]
	v_pk_mul_f32 v[116:117], v[116:117], v[164:165] op_sel_hi:[1,0]
	v_max_f32_e32 v114, 0, v114
	v_max_f32_e32 v115, 0, v115
	v_cvt_pk_bf16_f32 v123, v123, v124
	v_cvt_pk_bf16_f32 v124, v168, v127
	v_cvt_pk_bf16_f32 v125, v128, v125
	global_store_dwordx4 v163, v[122:125], s[10:11] nt
	v_max_f32_e32 v118, 0, v118
	v_max_f32_e32 v116, 0, v116
	v_mul_f32_e32 v122, v114, v114
	v_max_f32_e32 v114, 0, v119
	v_mul_f32_e32 v119, v115, v115
	v_max_f32_e32 v115, 0, v120
	v_mul_f32_e32 v118, v118, v118
	v_mul_f32_e32 v114, v114, v114
	v_mul_f32_e32 v115, v115, v115
	v_mul_f32_e32 v120, v116, v116
	v_max_f32_e32 v116, 0, v121
	v_max_f32_e32 v117, 0, v117
	v_mul_f32_e32 v116, v116, v116
	v_mul_f32_e32 v117, v117, v117
	v_cvt_pk_bf16_f32 v114, v118, v114
	v_cvt_pk_bf16_f32 v115, v115, v116
	v_or_b32_e32 v118, 0x100, v163
	v_cvt_pk_bf16_f32 v116, v122, v119
	v_cvt_pk_bf16_f32 v117, v120, v117
	global_store_dwordx4 v118, v[114:117], s[10:11] nt
	v_pk_mul_f32 v[90:91], v[90:91], v[166:167] op_sel_hi:[1,0]
	v_pk_mul_f32 v[94:95], v[94:95], v[166:167] op_sel_hi:[1,0]
	v_or_b32_e32 v115, 0x8000, v163
	v_mov_b32_e32 v114, v165
	v_pk_mul_f32 v[106:107], v[106:107], v[114:115] op_sel_hi:[1,0]
	v_pk_mul_f32 v[110:111], v[110:111], v[114:115] op_sel_hi:[1,0]
	v_pk_mul_f32 v[108:109], v[108:109], v[114:115] op_sel_hi:[1,0]
	v_max_f32_e32 v106, 0, v106
	v_pk_mul_f32 v[112:113], v[112:113], v[114:115] op_sel_hi:[1,0]
	v_mul_f32_e32 v116, v106, v106
	v_max_f32_e32 v106, 0, v111
	v_max_f32_e32 v107, 0, v107
	v_max_f32_e32 v108, 0, v108
	v_max_f32_e32 v110, 0, v110
	v_mul_f32_e32 v106, v106, v106
	v_mul_f32_e32 v111, v107, v107
	v_max_f32_e32 v107, 0, v112
	v_mul_f32_e32 v112, v108, v108
	v_max_f32_e32 v108, 0, v113
	v_max_f32_e32 v109, 0, v109
	v_pk_mul_f32 v[98:99], v[98:99], v[114:115] op_sel_hi:[1,0]
	v_mul_f32_e32 v110, v110, v110
	v_mul_f32_e32 v107, v107, v107
	v_mul_f32_e32 v108, v108, v108
	v_mul_f32_e32 v109, v109, v109
	v_cvt_pk_bf16_f32 v106, v110, v106
	v_pk_mul_f32 v[104:105], v[104:105], v[114:115] op_sel_hi:[1,0]
	v_pk_mul_f32 v[102:103], v[102:103], v[114:115] op_sel_hi:[1,0]
	v_pk_mul_f32 v[100:101], v[100:101], v[114:115] op_sel_hi:[1,0]
	v_max_f32_e32 v98, 0, v98
	v_max_f32_e32 v99, 0, v99
	v_cvt_pk_bf16_f32 v107, v107, v108
	v_cvt_pk_bf16_f32 v108, v116, v111
	v_cvt_pk_bf16_f32 v109, v112, v109
	global_store_dwordx4 v115, v[106:109], s[10:11]
	v_max_f32_e32 v102, 0, v102
	v_max_f32_e32 v100, 0, v100
	v_mul_f32_e32 v106, v98, v98
	v_max_f32_e32 v98, 0, v103
	v_mul_f32_e32 v103, v99, v99
	v_max_f32_e32 v99, 0, v104
	v_mul_f32_e32 v102, v102, v102
	v_mul_f32_e32 v98, v98, v98
	v_mul_f32_e32 v99, v99, v99
	v_mul_f32_e32 v104, v100, v100
	v_max_f32_e32 v100, 0, v105
	v_max_f32_e32 v101, 0, v101
	v_mul_f32_e32 v100, v100, v100
	v_mul_f32_e32 v101, v101, v101
	v_cvt_pk_bf16_f32 v98, v102, v98
	v_cvt_pk_bf16_f32 v99, v99, v100
	v_or_b32_e32 v102, 0x8100, v163
	v_pk_mul_f32 v[92:93], v[92:93], v[166:167] op_sel_hi:[1,0]
	v_max_f32_e32 v90, 0, v90
	v_cvt_pk_bf16_f32 v100, v106, v103
	v_cvt_pk_bf16_f32 v101, v104, v101
	global_store_dwordx4 v102, v[98:101], s[10:11]
	v_pk_mul_f32 v[96:97], v[96:97], v[166:167] op_sel_hi:[1,0]
	v_max_f32_e32 v91, 0, v91
	v_mul_f32_e32 v99, v90, v90
	v_max_f32_e32 v90, 0, v95
	v_max_f32_e32 v92, 0, v92
	v_max_f32_e32 v94, 0, v94
	v_mul_f32_e32 v90, v90, v90
	v_mul_f32_e32 v95, v91, v91
	v_max_f32_e32 v91, 0, v96
	v_mul_f32_e32 v96, v92, v92
	v_max_f32_e32 v92, 0, v97
	v_max_f32_e32 v93, 0, v93
	v_pk_mul_f32 v[82:83], v[82:83], v[166:167] op_sel_hi:[1,0]
	v_or_b32_e32 v98, 0x10000, v163
	v_mul_f32_e32 v94, v94, v94
	v_mul_f32_e32 v91, v91, v91
	v_mul_f32_e32 v92, v92, v92
	v_mul_f32_e32 v93, v93, v93
	v_cvt_pk_bf16_f32 v90, v94, v90
	v_pk_mul_f32 v[88:89], v[88:89], v[166:167] op_sel_hi:[1,0]
	v_pk_mul_f32 v[86:87], v[86:87], v[166:167] op_sel_hi:[1,0]
	v_pk_mul_f32 v[84:85], v[84:85], v[166:167] op_sel_hi:[1,0]
	v_max_f32_e32 v82, 0, v82
	v_max_f32_e32 v83, 0, v83
	v_cvt_pk_bf16_f32 v91, v91, v92
	v_cvt_pk_bf16_f32 v92, v99, v95
	v_cvt_pk_bf16_f32 v93, v96, v93
; #define PG8_GAS __attribute__((address_space(1)))
; #define PG8_PACK8(y0, y1) (u32x4){cvt_pk_bf16((y0)[0], (y0)[1]), cvt_pk_bf16((y0)[2], (y0)[3]), cvt_pk_bf16((y1)[0], (y1)[1]), cvt_pk_bf16((y1)[2], (y1)[3])}
;     __device__ __forceinline__ void operator()(const f32x4 (&acc)[2][2][4][2], const Unit& u, int ui, int wr, int wc, int fr, int fq) const {
;     ...
;         for (int ai = 0; ai < 2; ++ai)
; #pragma unroll
;             for (int m = 0; m < 4; ++m) {
;                 const unsigned row = row0 + ai * HALF + m * 16; const float rs = rsv[ai][m];
; #pragma unroll
;                 for (int bj = 0; bj < 2; ++bj) {
;                     f32x4 y0 = acc[ai][bj][m][0] * rs, y1 = acc[ai][bj][m][1] * rs;
; #pragma unroll
;                     for (int e = 0; e < 4; ++e) { const float a = fmaxf(y0[e], 0.f), b = fmaxf(y1[e], 0.f); y0[e] = a * a; y1[e] = b * b; }
;                     const u32x4 hw = PG8_PACK8(y0, y1);
;     ...
;                     if (probe_mode == 1) { asm volatile("" :: "v"(hw)); } else
;     ...
;                     *(PG8_GAS u32x4*)((PG8_GAS unsigned char*)ws + E_QKVO + (size_t)((unsigned)(u.pm >> 4) * (24u << 20) + (unsigned)(u.pn >> 2) * (8u << 20) + row * 2048u + (colp + bj * HALF) * 2u)) = hw;
	global_store_dwordx4 v98, v[90:93], s[10:11]
	v_max_f32_e32 v86, 0, v86
	v_max_f32_e32 v84, 0, v84
	v_mul_f32_e32 v90, v82, v82
	v_max_f32_e32 v82, 0, v87
	v_mul_f32_e32 v87, v83, v83
	v_max_f32_e32 v83, 0, v88
	v_mul_f32_e32 v86, v86, v86
	v_mul_f32_e32 v82, v82, v82
	v_mul_f32_e32 v83, v83, v83
	v_mul_f32_e32 v88, v84, v84
	v_max_f32_e32 v84, 0, v89
	v_max_f32_e32 v85, 0, v85
	v_mul_f32_e32 v84, v84, v84
	v_mul_f32_e32 v85, v85, v85
	v_cvt_pk_bf16_f32 v82, v86, v82
	v_cvt_pk_bf16_f32 v83, v83, v84
	v_or_b32_e32 v86, 0x10100, v163
	v_cvt_pk_bf16_f32 v84, v90, v87
	v_cvt_pk_bf16_f32 v85, v88, v85
	global_store_dwordx4 v86, v[82:85], s[10:11]
	v_pk_mul_f32 v[58:59], v[58:59], v[142:143] op_sel_hi:[1,0]
	v_pk_mul_f32 v[62:63], v[62:63], v[142:143] op_sel_hi:[1,0]
	v_or_b32_e32 v83, 0x18000, v163
	v_mov_b32_e32 v82, v167
	v_pk_mul_f32 v[74:75], v[74:75], v[82:83] op_sel_hi:[1,0]
	v_pk_mul_f32 v[78:79], v[78:79], v[82:83] op_sel_hi:[1,0]
	v_pk_mul_f32 v[76:77], v[76:77], v[82:83] op_sel_hi:[1,0]
	v_max_f32_e32 v74, 0, v74
	v_pk_mul_f32 v[80:81], v[80:81], v[82:83] op_sel_hi:[1,0]
	v_mul_f32_e32 v84, v74, v74
	v_max_f32_e32 v74, 0, v79
	v_max_f32_e32 v75, 0, v75
	v_max_f32_e32 v76, 0, v76
	v_max_f32_e32 v78, 0, v78
	v_mul_f32_e32 v74, v74, v74
	v_mul_f32_e32 v79, v75, v75
	v_max_f32_e32 v75, 0, v80
	v_mul_f32_e32 v80, v76, v76
	v_max_f32_e32 v76, 0, v81
	v_max_f32_e32 v77, 0, v77
	v_pk_mul_f32 v[66:67], v[66:67], v[82:83] op_sel_hi:[1,0]
	v_mul_f32_e32 v78, v78, v78
	v_mul_f32_e32 v75, v75, v75
	v_mul_f32_e32 v76, v76, v76
	v_mul_f32_e32 v77, v77, v77
	v_cvt_pk_bf16_f32 v74, v78, v74
	v_pk_mul_f32 v[72:73], v[72:73], v[82:83] op_sel_hi:[1,0]
	v_pk_mul_f32 v[70:71], v[70:71], v[82:83] op_sel_hi:[1,0]
	v_pk_mul_f32 v[68:69], v[68:69], v[82:83] op_sel_hi:[1,0]
	v_max_f32_e32 v66, 0, v66
	v_max_f32_e32 v67, 0, v67
	v_cvt_pk_bf16_f32 v75, v75, v76
	v_cvt_pk_bf16_f32 v76, v84, v79
	v_cvt_pk_bf16_f32 v77, v80, v77
	global_store_dwordx4 v83, v[74:77], s[10:11]
	v_max_f32_e32 v70, 0, v70
	v_max_f32_e32 v68, 0, v68
	v_mul_f32_e32 v74, v66, v66
	v_max_f32_e32 v66, 0, v71
	v_mul_f32_e32 v71, v67, v67
	v_max_f32_e32 v67, 0, v72
	v_mul_f32_e32 v70, v70, v70
	v_mul_f32_e32 v66, v66, v66
	v_mul_f32_e32 v67, v67, v67
	v_mul_f32_e32 v72, v68, v68
	v_max_f32_e32 v68, 0, v73
	v_max_f32_e32 v69, 0, v69
	v_mul_f32_e32 v68, v68, v68
	v_mul_f32_e32 v69, v69, v69
	v_cvt_pk_bf16_f32 v66, v70, v66
	v_cvt_pk_bf16_f32 v67, v67, v68
	v_or_b32_e32 v70, 0x18100, v163
	v_pk_mul_f32 v[60:61], v[60:61], v[142:143] op_sel_hi:[1,0]
	v_max_f32_e32 v58, 0, v58
	v_cvt_pk_bf16_f32 v68, v74, v71
	v_cvt_pk_bf16_f32 v69, v72, v69
	global_store_dwordx4 v70, v[66:69], s[10:11]
	v_pk_mul_f32 v[64:65], v[64:65], v[142:143] op_sel_hi:[1,0]
	v_max_f32_e32 v59, 0, v59
	v_mul_f32_e32 v67, v58, v58
	v_max_f32_e32 v58, 0, v63
	v_max_f32_e32 v60, 0, v60
	v_max_f32_e32 v62, 0, v62
	v_mul_f32_e32 v58, v58, v58
	v_mul_f32_e32 v63, v59, v59
	v_max_f32_e32 v59, 0, v64
	v_mul_f32_e32 v64, v60, v60
	v_max_f32_e32 v60, 0, v65
	v_max_f32_e32 v61, 0, v61
	v_pk_mul_f32 v[50:51], v[50:51], v[142:143] op_sel_hi:[1,0]
	v_add_u32_e32 v66, 0x40000, v163
	v_mul_f32_e32 v62, v62, v62
	v_mul_f32_e32 v59, v59, v59
	v_mul_f32_e32 v60, v60, v60
	v_mul_f32_e32 v61, v61, v61
	v_cvt_pk_bf16_f32 v58, v62, v58
	v_pk_mul_f32 v[56:57], v[56:57], v[142:143] op_sel_hi:[1,0]
	v_pk_mul_f32 v[54:55], v[54:55], v[142:143] op_sel_hi:[1,0]
	v_pk_mul_f32 v[52:53], v[52:53], v[142:143] op_sel_hi:[1,0]
	v_max_f32_e32 v50, 0, v50
	v_max_f32_e32 v51, 0, v51
	v_cvt_pk_bf16_f32 v59, v59, v60
	v_cvt_pk_bf16_f32 v60, v67, v63
	v_cvt_pk_bf16_f32 v61, v64, v61
	global_store_dwordx4 v66, v[58:61], s[10:11]
	v_max_f32_e32 v54, 0, v54
	v_max_f32_e32 v52, 0, v52
	v_mul_f32_e32 v58, v50, v50
	v_max_f32_e32 v50, 0, v55
	v_mul_f32_e32 v55, v51, v51
	v_max_f32_e32 v51, 0, v56
	v_mul_f32_e32 v54, v54, v54
	v_mul_f32_e32 v50, v50, v50
	v_mul_f32_e32 v51, v51, v51
	v_mul_f32_e32 v56, v52, v52
	v_max_f32_e32 v52, 0, v57
	v_max_f32_e32 v53, 0, v53
	v_mul_f32_e32 v52, v52, v52
	v_mul_f32_e32 v53, v53, v53
	v_cvt_pk_bf16_f32 v50, v54, v50
	v_cvt_pk_bf16_f32 v51, v51, v52
	v_add_u32_e32 v54, 0x40100, v163
	v_cvt_pk_bf16_f32 v52, v58, v55
	v_cvt_pk_bf16_f32 v53, v56, v53
	global_store_dwordx4 v54, v[50:53], s[10:11]
	v_pk_mul_f32 v[26:27], v[26:27], v[140:141] op_sel_hi:[1,0]
	v_pk_mul_f32 v[30:31], v[30:31], v[140:141] op_sel_hi:[1,0]
	v_add_u32_e32 v51, 0x48000, v163
	v_mov_b32_e32 v50, v143
	v_pk_mul_f32 v[42:43], v[42:43], v[50:51] op_sel_hi:[1,0]
	v_pk_mul_f32 v[46:47], v[46:47], v[50:51] op_sel_hi:[1,0]
	v_pk_mul_f32 v[44:45], v[44:45], v[50:51] op_sel_hi:[1,0]
	v_max_f32_e32 v42, 0, v42
	v_pk_mul_f32 v[48:49], v[48:49], v[50:51] op_sel_hi:[1,0]
	v_mul_f32_e32 v52, v42, v42
	v_max_f32_e32 v42, 0, v47
	v_max_f32_e32 v43, 0, v43
	v_max_f32_e32 v44, 0, v44
	v_max_f32_e32 v46, 0, v46
	v_mul_f32_e32 v42, v42, v42
	v_mul_f32_e32 v47, v43, v43
; #define PG8_GAS __attribute__((address_space(1)))
; #define PG8_PACK8(y0, y1) (u32x4){cvt_pk_bf16((y0)[0], (y0)[1]), cvt_pk_bf16((y0)[2], (y0)[3]), cvt_pk_bf16((y1)[0], (y1)[1]), cvt_pk_bf16((y1)[2], (y1)[3])}
; #define PG8_BAR __builtin_amdgcn_s_barrier()
;     __device__ __forceinline__ void operator()(const f32x4 (&acc)[2][2][4][2], const Unit& u, int ui, int wr, int wc, int fr, int fq) const {
;     ...
;         for (int ai = 0; ai < 2; ++ai)
; #pragma unroll
;             for (int m = 0; m < 4; ++m) {
;                 const unsigned row = row0 + ai * HALF + m * 16; const float rs = rsv[ai][m];
; #pragma unroll
;                 for (int bj = 0; bj < 2; ++bj) {
;                     f32x4 y0 = acc[ai][bj][m][0] * rs, y1 = acc[ai][bj][m][1] * rs;
; #pragma unroll
;                     for (int e = 0; e < 4; ++e) { const float a = fmaxf(y0[e], 0.f), b = fmaxf(y1[e], 0.f); y0[e] = a * a; y1[e] = b * b; }
;                     const u32x4 hw = PG8_PACK8(y0, y1);
;     ...
;                     if (probe_mode == 1) { asm volatile("" :: "v"(hw)); } else
;     ...
;                     *(PG8_GAS u32x4*)((PG8_GAS unsigned char*)ws + E_QKVO + (size_t)((unsigned)(u.pm >> 4) * (24u << 20) + (unsigned)(u.pn >> 2) * (8u << 20) + row * 2048u + (colp + bj * HALF) * 2u)) = hw;
; template <class Epi, class Sched, bool ALIGN_EPI = false, bool SP2 = false>
; __device__ __forceinline__ void gemm_phase(PG8_LAS unsigned char* lds, const Gemm g, const Sched& S, const Epi& E, const int tid) {
;     ...
;         if (!has_next) break;
; #pragma unroll
;         for (int a = 0; a < 2; ++a)
; #pragma unroll
;             for (int b = 0; b < 2; ++b)
; #pragma unroll
;                 for (int m = 0; m < 4; ++m)
; #pragma unroll
;                     for (int n = 0; n < 2; ++n) acc[a][b][m][n] = (f32x4){0.f, 0.f, 0.f, 0.f};
;         cur = nxt; cA = nA; cB = nB; ++ui;
;         if constexpr (ALIGN_EPI) { if (wr == 1) PG8_BAR; }
	v_max_f32_e32 v43, 0, v48
	v_mul_f32_e32 v48, v44, v44
	v_max_f32_e32 v44, 0, v49
	v_max_f32_e32 v45, 0, v45
	v_pk_mul_f32 v[34:35], v[34:35], v[50:51] op_sel_hi:[1,0]
	v_mul_f32_e32 v46, v46, v46
	v_mul_f32_e32 v43, v43, v43
	v_mul_f32_e32 v44, v44, v44
	v_mul_f32_e32 v45, v45, v45
	v_cvt_pk_bf16_f32 v42, v46, v42
	v_pk_mul_f32 v[40:41], v[40:41], v[50:51] op_sel_hi:[1,0]
	v_pk_mul_f32 v[38:39], v[38:39], v[50:51] op_sel_hi:[1,0]
	v_pk_mul_f32 v[36:37], v[36:37], v[50:51] op_sel_hi:[1,0]
	v_max_f32_e32 v34, 0, v34
	v_max_f32_e32 v35, 0, v35
	v_cvt_pk_bf16_f32 v43, v43, v44
	v_cvt_pk_bf16_f32 v44, v52, v47
	v_cvt_pk_bf16_f32 v45, v48, v45
	global_store_dwordx4 v51, v[42:45], s[10:11]
	v_max_f32_e32 v38, 0, v38
	v_max_f32_e32 v36, 0, v36
	v_mul_f32_e32 v42, v34, v34
	v_max_f32_e32 v34, 0, v39
	v_mul_f32_e32 v39, v35, v35
	v_max_f32_e32 v35, 0, v40
	v_mul_f32_e32 v38, v38, v38
	v_mul_f32_e32 v34, v34, v34
	v_mul_f32_e32 v35, v35, v35
	v_mul_f32_e32 v40, v36, v36
	v_max_f32_e32 v36, 0, v41
	v_max_f32_e32 v37, 0, v37
	v_mul_f32_e32 v36, v36, v36
	v_mul_f32_e32 v37, v37, v37
	v_cvt_pk_bf16_f32 v34, v38, v34
	v_cvt_pk_bf16_f32 v35, v35, v36
	v_add_u32_e32 v38, 0x48100, v163
	v_pk_mul_f32 v[28:29], v[28:29], v[140:141] op_sel_hi:[1,0]
	v_max_f32_e32 v26, 0, v26
	v_cvt_pk_bf16_f32 v36, v42, v39
	v_cvt_pk_bf16_f32 v37, v40, v37
	global_store_dwordx4 v38, v[34:37], s[10:11]
	v_pk_mul_f32 v[32:33], v[32:33], v[140:141] op_sel_hi:[1,0]
	v_max_f32_e32 v27, 0, v27
	v_mul_f32_e32 v35, v26, v26
	v_max_f32_e32 v26, 0, v31
	v_max_f32_e32 v28, 0, v28
	v_max_f32_e32 v30, 0, v30
	v_mul_f32_e32 v26, v26, v26
	v_mul_f32_e32 v31, v27, v27
	v_max_f32_e32 v27, 0, v32
	v_mul_f32_e32 v32, v28, v28
	v_max_f32_e32 v28, 0, v33
	v_max_f32_e32 v29, 0, v29
	v_pk_mul_f32 v[18:19], v[18:19], v[140:141] op_sel_hi:[1,0]
	v_add_u32_e32 v34, 0x50000, v163
	v_mul_f32_e32 v30, v30, v30
	v_mul_f32_e32 v27, v27, v27
	v_mul_f32_e32 v28, v28, v28
	v_mul_f32_e32 v29, v29, v29
	v_cvt_pk_bf16_f32 v26, v30, v26
	v_pk_mul_f32 v[24:25], v[24:25], v[140:141] op_sel_hi:[1,0]
	v_pk_mul_f32 v[22:23], v[22:23], v[140:141] op_sel_hi:[1,0]
	v_pk_mul_f32 v[20:21], v[20:21], v[140:141] op_sel_hi:[1,0]
	v_max_f32_e32 v18, 0, v18
	v_max_f32_e32 v19, 0, v19
	v_cvt_pk_bf16_f32 v27, v27, v28
	v_cvt_pk_bf16_f32 v28, v35, v31
	v_cvt_pk_bf16_f32 v29, v32, v29
	global_store_dwordx4 v34, v[26:29], s[10:11]
	v_max_f32_e32 v22, 0, v22
	v_max_f32_e32 v20, 0, v20
	v_mul_f32_e32 v26, v18, v18
	v_max_f32_e32 v18, 0, v23
	v_mul_f32_e32 v23, v19, v19
	v_max_f32_e32 v19, 0, v24
	v_mul_f32_e32 v22, v22, v22
	v_mul_f32_e32 v18, v18, v18
	v_mul_f32_e32 v19, v19, v19
	v_mul_f32_e32 v24, v20, v20
	v_max_f32_e32 v20, 0, v25
	v_max_f32_e32 v21, 0, v21
	v_mul_f32_e32 v20, v20, v20
	v_mul_f32_e32 v21, v21, v21
	v_cvt_pk_bf16_f32 v18, v22, v18
	v_cvt_pk_bf16_f32 v19, v19, v20
	v_add_u32_e32 v22, 0x50100, v163
	v_cvt_pk_bf16_f32 v20, v26, v23
	v_cvt_pk_bf16_f32 v21, v24, v21
	global_store_dwordx4 v22, v[18:21], s[10:11]
	s_andn2_b64 vcc, exec, s[0:1]
	s_mov_b64 s[0:1], -1
	v_add_u32_e32 v19, 0x58000, v163
	v_mov_b32_e32 v18, v141
	v_pk_mul_f32 v[10:11], v[10:11], v[18:19] op_sel_hi:[1,0]
	v_pk_mul_f32 v[14:15], v[14:15], v[18:19] op_sel_hi:[1,0]
	v_pk_mul_f32 v[12:13], v[12:13], v[18:19] op_sel_hi:[1,0]
	v_max_f32_e32 v10, 0, v10
	v_pk_mul_f32 v[16:17], v[16:17], v[18:19] op_sel_hi:[1,0]
	v_mul_f32_e32 v20, v10, v10
	v_max_f32_e32 v10, 0, v15
	v_max_f32_e32 v11, 0, v11
	v_max_f32_e32 v12, 0, v12
	v_max_f32_e32 v14, 0, v14
	v_mul_f32_e32 v10, v10, v10
	v_mul_f32_e32 v15, v11, v11
	v_max_f32_e32 v11, 0, v16
	v_mul_f32_e32 v16, v12, v12
	v_max_f32_e32 v12, 0, v17
	v_max_f32_e32 v13, 0, v13
	v_pk_mul_f32 v[2:3], v[2:3], v[18:19] op_sel_hi:[1,0]
	v_mul_f32_e32 v14, v14, v14
	v_mul_f32_e32 v11, v11, v11
	v_mul_f32_e32 v12, v12, v12
	v_mul_f32_e32 v13, v13, v13
	v_cvt_pk_bf16_f32 v10, v14, v10
	v_pk_mul_f32 v[6:7], v[6:7], v[18:19] op_sel_hi:[1,0]
	v_pk_mul_f32 v[4:5], v[4:5], v[18:19] op_sel_hi:[1,0]
	v_max_f32_e32 v2, 0, v2
	v_cvt_pk_bf16_f32 v11, v11, v12
	v_cvt_pk_bf16_f32 v12, v20, v15
	v_cvt_pk_bf16_f32 v13, v16, v13
	global_store_dwordx4 v19, v[10:13], s[10:11]
	v_pk_mul_f32 v[8:9], v[8:9], v[18:19] op_sel_hi:[1,0]
	v_max_f32_e32 v6, 0, v6
	v_mul_f32_e32 v10, v2, v2
	v_max_f32_e32 v2, 0, v7
	v_max_f32_e32 v3, 0, v3
	v_max_f32_e32 v4, 0, v4
	v_mul_f32_e32 v6, v6, v6
	v_mul_f32_e32 v2, v2, v2
	v_mul_f32_e32 v7, v3, v3
	v_max_f32_e32 v3, 0, v8
	v_mul_f32_e32 v8, v4, v4
	v_max_f32_e32 v4, 0, v9
	v_max_f32_e32 v5, 0, v5
	v_mul_f32_e32 v3, v3, v3
	v_mul_f32_e32 v4, v4, v4
	v_mul_f32_e32 v5, v5, v5
	v_cvt_pk_bf16_f32 v2, v6, v2
	v_add_u32_e32 v6, 0x58100, v163
	v_cvt_pk_bf16_f32 v3, v3, v4
	v_cvt_pk_bf16_f32 v4, v10, v7
	v_cvt_pk_bf16_f32 v5, v8, v5
	global_store_dwordx4 v6, v[2:5], s[10:11]
	s_mov_b32 s100, 2
	s_cbranch_vccnz .LBB0_53
	s_andn2_b64 vcc, exec, s[6:7]
	s_cbranch_vccnz .LBB0_52
	s_barrier
	s_branch .LBB0_52
